# nt (streaming) cache hint on the read-once f32 weight loads of the prologue and per-layer expert weight conversion loops
# speedup vs baseline: 1.0160x; 1.0120x over previous
; __device__ __forceinline__ void cvt_load(const CvtItem& it, float (&v)[32], int lane) {
; #pragma unroll
;     for (int i = 0; i < 32; ++i) { const int kk = 2 * i + (lane >> 5); v[i] = it.W[(size_t)(it.k0 + kk) * it.N + it.n0 + (lane & 31)]; }
; }
; template <int PH, bool PRB = false>
; __device__ __forceinline__ void run_phase(int layer, LAS unsigned char* lds, const int wv_) {
;     ...
;             constexpr int NITEMS = 13056 + 4096; int gi = gw;
;             if (gi < NITEMS) { CvtItem cur = item_of(gi); float v[32]; cvt_load(cur, v, lane);
;                 for (;;) { const int gn = gi + NGW; const bool more = gn < NITEMS; CvtItem nxt = item_of(more ? gn : gi); float vn[32];
;                     if (more) cvt_load(nxt, vn, lane);
;                     cvt_finish(cur, v, scr, lane);
;                     if (!more) break;
; #pragma unroll
;                     for (int i = 0; i < 32; ++i) v[i] = vn[i];
;                     cur = nxt; gi = gn; } }
.LBB0_104:
	s_ashr_i32 s41, s40, 31
	v_lshrrev_b32_e32 v67, 5, v1
	s_lshl_b64 s[8:9], s[40:41], 2
	v_add_u32_e32 v35, s30, v67
	v_and_b32_e32 v36, 31, v56
	s_add_u32 s6, s6, s8
	v_mov_b32_e32 v69, 0
	s_addc_u32 s7, s7, s9
	v_lshlrev_b32_e32 v68, 2, v36
	v_ashrrev_i32_e32 v2, 31, v35
	v_lshl_add_u64 v[26:27], s[6:7], 0, v[68:69]
	v_mul_lo_u32 v4, s4, v2
	v_mul_lo_u32 v5, s5, v35
	v_mad_u64_u32 v[2:3], s[6:7], s4, v35, 0
	v_add3_u32 v3, v3, v4, v5
	v_add_u32_e32 v4, 2, v35
	v_ashrrev_i32_e32 v5, 31, v4
	v_mul_lo_u32 v6, s4, v5
	v_mul_lo_u32 v7, s5, v4
	v_mad_u64_u32 v[4:5], s[6:7], s4, v4, 0
	v_add3_u32 v5, v5, v6, v7
	v_add_u32_e32 v6, 4, v35
	v_ashrrev_i32_e32 v7, 31, v6
	v_mul_lo_u32 v8, s4, v7
	v_mul_lo_u32 v9, s5, v6
	v_mad_u64_u32 v[6:7], s[6:7], s4, v6, 0
	v_add3_u32 v7, v7, v8, v9
	v_add_u32_e32 v8, 6, v35
	v_ashrrev_i32_e32 v9, 31, v8
	v_mul_lo_u32 v10, s4, v9
	v_mul_lo_u32 v11, s5, v8
	v_mad_u64_u32 v[8:9], s[6:7], s4, v8, 0
	v_add3_u32 v9, v9, v10, v11
	v_add_u32_e32 v10, 8, v35
	v_ashrrev_i32_e32 v11, 31, v10
	v_mul_lo_u32 v12, s4, v11
	v_mul_lo_u32 v13, s5, v10
	v_mad_u64_u32 v[10:11], s[6:7], s4, v10, 0
	v_add3_u32 v11, v11, v12, v13
	v_add_u32_e32 v12, 10, v35
	v_ashrrev_i32_e32 v13, 31, v12
	v_mul_lo_u32 v14, s4, v13
	v_mul_lo_u32 v15, s5, v12
	v_mad_u64_u32 v[12:13], s[6:7], s4, v12, 0
	v_add3_u32 v13, v13, v14, v15
	v_add_u32_e32 v14, 12, v35
	v_ashrrev_i32_e32 v15, 31, v14
	v_mul_lo_u32 v16, s4, v15
	v_mul_lo_u32 v17, s5, v14
	v_mad_u64_u32 v[14:15], s[6:7], s4, v14, 0
	v_add3_u32 v15, v15, v16, v17
	v_add_u32_e32 v16, 14, v35
	v_ashrrev_i32_e32 v17, 31, v16
	v_mul_lo_u32 v18, s4, v17
	v_mul_lo_u32 v19, s5, v16
	v_mad_u64_u32 v[16:17], s[6:7], s4, v16, 0
	v_lshl_add_u64 v[2:3], v[2:3], 2, v[26:27]
	v_lshl_add_u64 v[4:5], v[4:5], 2, v[26:27]
	v_lshl_add_u64 v[6:7], v[6:7], 2, v[26:27]
	v_lshl_add_u64 v[8:9], v[8:9], 2, v[26:27]
	v_lshl_add_u64 v[10:11], v[10:11], 2, v[26:27]
	v_add3_u32 v17, v17, v18, v19
	v_lshl_add_u64 v[12:13], v[12:13], 2, v[26:27]
	v_lshl_add_u64 v[14:15], v[14:15], 2, v[26:27]
	v_lshl_add_u64 v[16:17], v[16:17], 2, v[26:27]
	global_load_dword v2, v[2:3], off nt
	s_nop 0
	global_load_dword v3, v[4:5], off nt
	s_nop 0
	global_load_dword v4, v[6:7], off nt
	global_load_dword v5, v[8:9], off nt
	s_nop 0
	global_load_dword v6, v[10:11], off nt
	global_load_dword v7, v[12:13], off nt
	global_load_dword v8, v[14:15], off nt
	global_load_dword v9, v[16:17], off nt
	v_add_u32_e32 v10, 16, v35
	v_ashrrev_i32_e32 v11, 31, v10
	v_mul_lo_u32 v12, s4, v11
	v_mul_lo_u32 v13, s5, v10
	v_mad_u64_u32 v[10:11], s[6:7], s4, v10, 0
	v_add3_u32 v11, v11, v12, v13
	v_add_u32_e32 v12, 18, v35
	v_ashrrev_i32_e32 v13, 31, v12
	v_mul_lo_u32 v14, s4, v13
	v_mul_lo_u32 v15, s5, v12
	v_mad_u64_u32 v[12:13], s[6:7], s4, v12, 0
	v_add3_u32 v13, v13, v14, v15
	v_add_u32_e32 v14, 20, v35
	v_ashrrev_i32_e32 v15, 31, v14
	v_mul_lo_u32 v16, s4, v15
	v_mul_lo_u32 v17, s5, v14
	v_mad_u64_u32 v[14:15], s[6:7], s4, v14, 0
	v_add3_u32 v15, v15, v16, v17
	v_add_u32_e32 v16, 22, v35
	v_ashrrev_i32_e32 v17, 31, v16
	v_mul_lo_u32 v18, s4, v17
	v_mul_lo_u32 v19, s5, v16
	v_mad_u64_u32 v[16:17], s[6:7], s4, v16, 0
	v_add3_u32 v17, v17, v18, v19
	v_add_u32_e32 v18, 24, v35
	v_ashrrev_i32_e32 v19, 31, v18
	v_mul_lo_u32 v20, s4, v19
	v_mul_lo_u32 v21, s5, v18
	v_mad_u64_u32 v[18:19], s[6:7], s4, v18, 0
	v_add3_u32 v19, v19, v20, v21
	v_add_u32_e32 v20, 26, v35
	v_ashrrev_i32_e32 v21, 31, v20
	v_mul_lo_u32 v22, s4, v21
	v_mul_lo_u32 v23, s5, v20
	v_mad_u64_u32 v[20:21], s[6:7], s4, v20, 0
	v_add3_u32 v21, v21, v22, v23
	v_add_u32_e32 v22, 28, v35
	v_ashrrev_i32_e32 v23, 31, v22
	v_mul_lo_u32 v24, s4, v23
	v_mul_lo_u32 v25, s5, v22
	v_mad_u64_u32 v[22:23], s[6:7], s4, v22, 0
	v_add3_u32 v23, v23, v24, v25
	v_add_u32_e32 v24, 30, v35
	v_ashrrev_i32_e32 v25, 31, v24
	v_mul_lo_u32 v28, s4, v25
	v_mul_lo_u32 v29, s5, v24
	v_mad_u64_u32 v[24:25], s[6:7], s4, v24, 0
	v_add3_u32 v25, v25, v28, v29
	v_lshl_add_u64 v[10:11], v[10:11], 2, v[26:27]
	v_lshl_add_u64 v[12:13], v[12:13], 2, v[26:27]
	v_lshl_add_u64 v[14:15], v[14:15], 2, v[26:27]
	v_lshl_add_u64 v[16:17], v[16:17], 2, v[26:27]
	v_lshl_add_u64 v[18:19], v[18:19], 2, v[26:27]
	v_lshl_add_u64 v[20:21], v[20:21], 2, v[26:27]
	v_lshl_add_u64 v[22:23], v[22:23], 2, v[26:27]
	v_lshl_add_u64 v[24:25], v[24:25], 2, v[26:27]
	global_load_dword v10, v[10:11], off nt
	s_nop 0
	global_load_dword v11, v[12:13], off nt
	s_nop 0
	global_load_dword v12, v[14:15], off nt
	global_load_dword v13, v[16:17], off nt
	s_nop 0
	global_load_dword v14, v[18:19], off nt
	global_load_dword v15, v[20:21], off nt
	global_load_dword v16, v[22:23], off nt
	global_load_dword v17, v[24:25], off nt
	v_add_u32_e32 v18, 32, v35
	v_ashrrev_i32_e32 v19, 31, v18
	v_mul_lo_u32 v20, s4, v19
	v_mul_lo_u32 v21, s5, v18
	v_mad_u64_u32 v[18:19], s[6:7], s4, v18, 0
	v_add3_u32 v19, v19, v20, v21
	v_add_u32_e32 v20, 34, v35
	v_ashrrev_i32_e32 v21, 31, v20
	v_mul_lo_u32 v22, s4, v21
	v_mul_lo_u32 v23, s5, v20
	v_mad_u64_u32 v[20:21], s[6:7], s4, v20, 0
; #define LAS __attribute__((address_space(3)))
; #define CVT_PK_FP8_SAT(a, b, old, hi) __builtin_amdgcn_cvt_pk_fp8_f32(__builtin_amdgcn_fmed3f((a), -448.0f, 448.0f), __builtin_amdgcn_fmed3f((b), -448.0f, 448.0f), (old), (hi))
; __device__ __forceinline__ void cvt_load(const CvtItem& it, float (&v)[32], int lane) {
; #pragma unroll
;     for (int i = 0; i < 32; ++i) { const int kk = 2 * i + (lane >> 5); v[i] = it.W[(size_t)(it.k0 + kk) * it.N + it.n0 + (lane & 31)]; }
; }
; __device__ __forceinline__ void cvt_finish(const CvtItem& it, float (&v)[32], LAS float* scr, int lane) {
;     if (it.g) { const float gv = it.g[it.k0 + lane];
; #pragma unroll
;         for (int i = 0; i < 32; ++i) { const float g0 = __builtin_bit_cast(float, __builtin_amdgcn_readlane(__builtin_bit_cast(int, gv), 2 * i)), g1 = __builtin_bit_cast(float, __builtin_amdgcn_readlane(__builtin_bit_cast(int, gv), 2 * i + 1)); v[i] *= (lane >> 5) ? g1 : g0; } }
; #pragma unroll
;     for (int i = 0; i < 32; ++i) { const int kk = 2 * i + (lane >> 5); scr[kk * 33 + (lane & 31)] = v[i]; }
;     asm volatile("s_waitcnt lgkmcnt(0)" ::: "memory");
;     const int c = lane & 7;
; #pragma unroll
;     for (int j = 0; j < 4; ++j) { const int n = it.n0 + (lane >> 3) + 8 * j; const LAS float* s = scr + (8 * c) * 33 + (lane >> 3) + 8 * j;
;         const int row = it.rowmode == 0 ? n : ((n >> 7) * 256 + (it.rowmode == 2 ? 128 : 0) + (n & 127));
;         if (it.fp8) { int w0 = CVT_PK_FP8_SAT(s[0 * 33] * FP8_WSCALE, s[1 * 33] * FP8_WSCALE, 0, false); w0 = CVT_PK_FP8_SAT(s[2 * 33] * FP8_WSCALE, s[3 * 33] * FP8_WSCALE, w0, true);
;             int w1 = CVT_PK_FP8_SAT(s[4 * 33] * FP8_WSCALE, s[5 * 33] * FP8_WSCALE, 0, false); w1 = CVT_PK_FP8_SAT(s[6 * 33] * FP8_WSCALE, s[7 * 33] * FP8_WSCALE, w1, true);
	v_add3_u32 v21, v21, v22, v23
	v_add_u32_e32 v22, 36, v35
	v_ashrrev_i32_e32 v23, 31, v22
	v_mul_lo_u32 v24, s4, v23
	v_mul_lo_u32 v25, s5, v22
	v_mad_u64_u32 v[22:23], s[6:7], s4, v22, 0
	v_add3_u32 v23, v23, v24, v25
	v_add_u32_e32 v24, 38, v35
	v_ashrrev_i32_e32 v25, 31, v24
	v_mul_lo_u32 v28, s4, v25
	v_mul_lo_u32 v29, s5, v24
	v_mad_u64_u32 v[24:25], s[6:7], s4, v24, 0
	v_add3_u32 v25, v25, v28, v29
	v_add_u32_e32 v28, 40, v35
	v_ashrrev_i32_e32 v29, 31, v28
	v_mul_lo_u32 v30, s4, v29
	v_mul_lo_u32 v31, s5, v28
	v_mad_u64_u32 v[28:29], s[6:7], s4, v28, 0
	v_add3_u32 v29, v29, v30, v31
	v_add_u32_e32 v30, 42, v35
	v_ashrrev_i32_e32 v31, 31, v30
	v_mul_lo_u32 v32, s4, v31
	v_mul_lo_u32 v33, s5, v30
	v_mad_u64_u32 v[30:31], s[6:7], s4, v30, 0
	v_add3_u32 v31, v31, v32, v33
	v_add_u32_e32 v32, 44, v35
	v_ashrrev_i32_e32 v33, 31, v32
	v_mul_lo_u32 v37, s4, v33
	v_mul_lo_u32 v38, s5, v32
	v_mad_u64_u32 v[32:33], s[6:7], s4, v32, 0
	v_add3_u32 v33, v33, v37, v38
	v_add_u32_e32 v37, 46, v35
	v_ashrrev_i32_e32 v38, 31, v37
	v_mul_lo_u32 v40, s4, v38
	v_mul_lo_u32 v41, s5, v37
	v_mad_u64_u32 v[38:39], s[6:7], s4, v37, 0
	v_add3_u32 v39, v39, v40, v41
	v_lshl_add_u64 v[18:19], v[18:19], 2, v[26:27]
	v_lshl_add_u64 v[20:21], v[20:21], 2, v[26:27]
	v_lshl_add_u64 v[22:23], v[22:23], 2, v[26:27]
	v_lshl_add_u64 v[24:25], v[24:25], 2, v[26:27]
	v_lshl_add_u64 v[28:29], v[28:29], 2, v[26:27]
	v_lshl_add_u64 v[30:31], v[30:31], 2, v[26:27]
	v_lshl_add_u64 v[32:33], v[32:33], 2, v[26:27]
	v_lshl_add_u64 v[38:39], v[38:39], 2, v[26:27]
	global_load_dword v18, v[18:19], off nt
	s_nop 0
	global_load_dword v19, v[20:21], off nt
	s_nop 0
	global_load_dword v20, v[22:23], off nt
	global_load_dword v21, v[24:25], off nt
	s_nop 0
	global_load_dword v22, v[28:29], off nt
	global_load_dword v23, v[30:31], off nt
	global_load_dword v24, v[32:33], off nt
	global_load_dword v25, v[38:39], off nt
	v_add_u32_e32 v28, 48, v35
	v_ashrrev_i32_e32 v29, 31, v28
	v_mul_lo_u32 v30, s4, v29
	v_mul_lo_u32 v31, s5, v28
	v_mad_u64_u32 v[28:29], s[6:7], s4, v28, 0
	v_add3_u32 v29, v29, v30, v31
	v_add_u32_e32 v30, 50, v35
	v_ashrrev_i32_e32 v31, 31, v30
	v_mul_lo_u32 v32, s4, v31
	v_mul_lo_u32 v33, s5, v30
	v_mad_u64_u32 v[30:31], s[6:7], s4, v30, 0
	v_add3_u32 v31, v31, v32, v33
	v_add_u32_e32 v32, 52, v35
	v_ashrrev_i32_e32 v33, 31, v32
	v_mul_lo_u32 v37, s4, v33
	v_mul_lo_u32 v38, s5, v32
	v_mad_u64_u32 v[32:33], s[6:7], s4, v32, 0
	v_add3_u32 v33, v33, v37, v38
	v_add_u32_e32 v37, 54, v35
	v_ashrrev_i32_e32 v38, 31, v37
	v_mul_lo_u32 v40, s4, v38
	v_mul_lo_u32 v41, s5, v37
	v_mad_u64_u32 v[38:39], s[6:7], s4, v37, 0
	v_add_u32_e32 v37, 56, v35
	v_add3_u32 v39, v39, v40, v41
	v_ashrrev_i32_e32 v40, 31, v37
	v_mul_lo_u32 v42, s4, v40
	v_mul_lo_u32 v43, s5, v37
	v_mad_u64_u32 v[40:41], s[6:7], s4, v37, 0
	v_add_u32_e32 v37, 58, v35
	v_add3_u32 v41, v41, v42, v43
	v_ashrrev_i32_e32 v42, 31, v37
	v_mul_lo_u32 v44, s4, v42
	v_mul_lo_u32 v45, s5, v37
	v_mad_u64_u32 v[42:43], s[6:7], s4, v37, 0
	v_add_u32_e32 v37, 60, v35
	v_add3_u32 v43, v43, v44, v45
	v_ashrrev_i32_e32 v44, 31, v37
	v_add_u32_e32 v35, 62, v35
	v_mul_lo_u32 v46, s4, v44
	v_mul_lo_u32 v47, s5, v37
	v_mad_u64_u32 v[44:45], s[6:7], s4, v37, 0
	v_ashrrev_i32_e32 v37, 31, v35
	v_add3_u32 v45, v45, v46, v47
	v_mul_lo_u32 v37, s4, v37
	v_mul_lo_u32 v48, s5, v35
	v_mad_u64_u32 v[46:47], s[4:5], s4, v35, 0
	v_lshl_add_u64 v[28:29], v[28:29], 2, v[26:27]
	v_lshl_add_u64 v[30:31], v[30:31], 2, v[26:27]
	v_lshl_add_u64 v[32:33], v[32:33], 2, v[26:27]
	v_add3_u32 v47, v47, v37, v48
	v_lshl_add_u64 v[38:39], v[38:39], 2, v[26:27]
	v_lshl_add_u64 v[40:41], v[40:41], 2, v[26:27]
	v_lshl_add_u64 v[42:43], v[42:43], 2, v[26:27]
	v_lshl_add_u64 v[44:45], v[44:45], 2, v[26:27]
	v_lshl_add_u64 v[46:47], v[46:47], 2, v[26:27]
	global_load_dword v26, v[28:29], off nt
	global_load_dword v27, v[30:31], off nt
	s_nop 0
	global_load_dword v28, v[32:33], off nt
	global_load_dword v29, v[38:39], off nt
	global_load_dword v30, v[40:41], off nt
	global_load_dword v31, v[42:43], off nt
	s_nop 0
	global_load_dword v32, v[44:45], off nt
	global_load_dword v33, v[46:47], off nt
	s_add_u32 s41, s44, 0x1e000000
	s_addc_u32 s48, s45, 0
	s_add_u32 s49, s44, 0x1d800000
	s_addc_u32 s60, s45, 0
	s_add_u32 s61, s44, 0x1d400000
	s_addc_u32 s62, s45, 0
	s_add_u32 s63, s44, 0x1d000000
	s_addc_u32 s64, s45, 0
	s_add_u32 s65, s44, 0x100000
	s_addc_u32 s66, s45, 0
	s_add_u32 s67, s44, 0x1a800000
	v_readlane_b32 s6, v254, 9
	s_addc_u32 s68, s45, 0
	v_lshrrev_b32_e32 v74, 3, v1
	v_and_b32_e32 v70, 56, v34
	v_add_u32_e32 v35, s6, v68
	v_mul_u32_u24_e32 v37, 0x84, v67
	s_add_u32 s69, s44, 0x1300000
	v_mul_u32_u24_e32 v34, 0x84, v70
	v_lshlrev_b32_e32 v38, 2, v74
	s_addc_u32 s70, s45, 0
	v_cmp_gt_u32_e64 s[4:5], 32, v1
	v_add3_u32 v75, s6, v34, v38
	v_mov_b32_e32 v71, v69
	v_or_b32_e32 v76, 8, v74
	v_or_b32_e32 v77, 16, v74
	v_or_b32_e32 v78, 24, v74
	v_lshlrev_b32_e32 v68, 2, v36
	v_add_u32_e32 v79, v35, v37
	s_mov_b32 s71, 0xc3e00000
	v_mov_b32_e32 v80, 0x43e00000
	s_branch .LBB0_106

; #define LAS __attribute__((address_space(3)))
; __device__ __forceinline__ void cvt_finish(const CvtItem& it, float (&v)[32], LAS float* scr, int lane) {
;     if (it.g) { const float gv = it.g[it.k0 + lane];
; #pragma unroll
;         for (int i = 0; i < 32; ++i) { const float g0 = __builtin_bit_cast(float, __builtin_amdgcn_readlane(__builtin_bit_cast(int, gv), 2 * i)), g1 = __builtin_bit_cast(float, __builtin_amdgcn_readlane(__builtin_bit_cast(int, gv), 2 * i + 1)); v[i] *= (lane >> 5) ? g1 : g0; } }
.LBB0_129:
	v_add_u32_e32 v72, s30, v1
	v_ashrrev_i32_e32 v73, 31, v72
	v_lshl_add_u64 v[72:73], v[72:73], 2, s[42:43]
	global_load_dword v72, v[72:73], off nt
	s_waitcnt vmcnt(0)
	v_readlane_b32 s8, v72, 0
	v_readlane_b32 s9, v72, 1
	v_readlane_b32 s31, v72, 2
	v_readlane_b32 s51, v72, 3
	v_mov_b32_e32 v73, s9
	v_mov_b32_e32 v81, s8
	s_waitcnt lgkmcnt(0)
	v_mov_b32_e32 v82, s51
	v_mov_b32_e32 v83, s31
	v_cndmask_b32_e64 v73, v73, v81, s[4:5]
	v_cndmask_b32_e64 v81, v82, v83, s[4:5]
	v_readlane_b32 s8, v72, 28
	v_readlane_b32 s9, v72, 29
	v_mul_f32_e32 v2, v2, v73
	v_mul_f32_e32 v3, v3, v81
	v_mov_b32_e32 v73, s9
	v_mov_b32_e32 v81, s8
	v_cndmask_b32_e64 v73, v73, v81, s[4:5]
	v_readlane_b32 s8, v72, 30
	v_readlane_b32 s9, v72, 31
	v_mul_f32_e32 v16, v16, v73
	v_mov_b32_e32 v81, s8
	v_mov_b32_e32 v73, s9
	v_cndmask_b32_e64 v73, v73, v81, s[4:5]
	v_readlane_b32 s8, v72, 32
	v_readlane_b32 s9, v72, 33
	v_mul_f32_e32 v17, v17, v73
	v_mov_b32_e32 v81, s8
	v_mov_b32_e32 v73, s9
	v_cndmask_b32_e64 v73, v73, v81, s[4:5]
	v_readlane_b32 s8, v72, 34
	v_readlane_b32 s9, v72, 35
	v_mul_f32_e32 v18, v18, v73
	v_mov_b32_e32 v81, s8
	v_mov_b32_e32 v73, s9
	v_cndmask_b32_e64 v73, v73, v81, s[4:5]
	v_readlane_b32 s8, v72, 36
	v_readlane_b32 s9, v72, 37
	v_mul_f32_e32 v19, v19, v73
	v_mov_b32_e32 v81, s8
	v_mov_b32_e32 v73, s9
	v_cndmask_b32_e64 v73, v73, v81, s[4:5]
	v_readlane_b32 s8, v72, 38
	v_readlane_b32 s9, v72, 39
	v_mul_f32_e32 v20, v20, v73
	v_mov_b32_e32 v81, s8
	v_mov_b32_e32 v73, s9
	v_cndmask_b32_e64 v73, v73, v81, s[4:5]
	v_readlane_b32 s8, v72, 40
	v_readlane_b32 s9, v72, 41
	v_mul_f32_e32 v21, v21, v73
	v_mov_b32_e32 v81, s8
	v_mov_b32_e32 v73, s9
	v_cndmask_b32_e64 v73, v73, v81, s[4:5]
	v_readlane_b32 s8, v72, 42
	v_readlane_b32 s9, v72, 43
	v_mul_f32_e32 v22, v22, v73
	v_mov_b32_e32 v81, s8
	v_mov_b32_e32 v73, s9
	v_cndmask_b32_e64 v73, v73, v81, s[4:5]
	v_readlane_b32 s8, v72, 44
	v_readlane_b32 s9, v72, 45
	v_mul_f32_e32 v23, v23, v73
	v_mov_b32_e32 v81, s8
	v_mov_b32_e32 v73, s9
	v_cndmask_b32_e64 v73, v73, v81, s[4:5]
	v_readlane_b32 s8, v72, 46
	v_readlane_b32 s9, v72, 47
	v_mul_f32_e32 v24, v24, v73
	v_mov_b32_e32 v81, s8
	v_mov_b32_e32 v73, s9
	v_cndmask_b32_e64 v73, v73, v81, s[4:5]
	v_readlane_b32 s8, v72, 48
	v_readlane_b32 s9, v72, 49
	v_mul_f32_e32 v25, v25, v73
	v_mov_b32_e32 v81, s8
	v_mov_b32_e32 v73, s9
	v_cndmask_b32_e64 v73, v73, v81, s[4:5]
	v_readlane_b32 s8, v72, 50
	v_readlane_b32 s9, v72, 51
	v_mul_f32_e32 v26, v26, v73
	v_mov_b32_e32 v81, s8
	v_mov_b32_e32 v73, s9
	v_cndmask_b32_e64 v73, v73, v81, s[4:5]
	v_readlane_b32 s8, v72, 52
	v_readlane_b32 s9, v72, 53
	v_mul_f32_e32 v27, v27, v73
	v_mov_b32_e32 v81, s8
	v_mov_b32_e32 v73, s9
	v_cndmask_b32_e64 v73, v73, v81, s[4:5]
	v_readlane_b32 s8, v72, 54
	v_readlane_b32 s9, v72, 55
	v_mul_f32_e32 v28, v28, v73
	v_mov_b32_e32 v81, s8
	v_mov_b32_e32 v73, s9
	v_cndmask_b32_e64 v73, v73, v81, s[4:5]
	v_readlane_b32 s8, v72, 56
	v_readlane_b32 s9, v72, 57
	v_mul_f32_e32 v29, v29, v73
	v_mov_b32_e32 v81, s8
	v_mov_b32_e32 v73, s9
	v_cndmask_b32_e64 v73, v73, v81, s[4:5]
	v_readlane_b32 s8, v72, 58
	v_readlane_b32 s9, v72, 59
	v_mul_f32_e32 v30, v30, v73
	v_mov_b32_e32 v81, s8
	v_mov_b32_e32 v73, s9
	v_cndmask_b32_e64 v73, v73, v81, s[4:5]
	v_readlane_b32 s8, v72, 60
	v_readlane_b32 s9, v72, 61
	v_mul_f32_e32 v31, v31, v73
	v_mov_b32_e32 v81, s8
	v_mov_b32_e32 v73, s9
	v_readlane_b32 s54, v72, 4
	v_readlane_b32 s55, v72, 5
	v_readlane_b32 s56, v72, 6
	v_readlane_b32 s57, v72, 7
	v_readlane_b32 s59, v72, 8
	v_readlane_b32 s74, v72, 9
	v_readlane_b32 s75, v72, 10
	v_readlane_b32 s76, v72, 11
	v_readlane_b32 s77, v72, 12
	v_readlane_b32 s78, v72, 13
	v_readlane_b32 s79, v72, 14
	v_readlane_b32 s80, v72, 15
	v_readlane_b32 s81, v72, 16
	v_readlane_b32 s82, v72, 17
	v_readlane_b32 s83, v72, 18
	v_readlane_b32 s84, v72, 19
	v_readlane_b32 s85, v72, 20
	v_readlane_b32 s86, v72, 21
	v_readlane_b32 s87, v72, 22
	v_readlane_b32 s88, v72, 23
	v_readlane_b32 s89, v72, 24
	v_readlane_b32 s90, v72, 25
	v_readlane_b32 s91, v72, 26
	v_readlane_b32 s92, v72, 27
	v_cndmask_b32_e64 v73, v73, v81, s[4:5]
	v_readlane_b32 s8, v72, 62
	v_readlane_b32 s9, v72, 63
	v_mov_b32_e32 v84, s55
	v_mov_b32_e32 v85, s54
	v_mov_b32_e32 v86, s57
	v_mov_b32_e32 v87, s56
	v_mov_b32_e32 v88, s74
	v_mov_b32_e32 v89, s59
	v_mov_b32_e32 v90, s76
	v_mov_b32_e32 v91, s75
	v_mov_b32_e32 v92, s78
	v_mov_b32_e32 v93, s77
	v_mov_b32_e32 v94, s80
	v_mov_b32_e32 v95, s79
	v_mov_b32_e32 v96, s82
	v_mov_b32_e32 v97, s81
	v_mov_b32_e32 v98, s84
	v_mov_b32_e32 v99, s83
	v_mov_b32_e32 v100, s86
	v_mov_b32_e32 v101, s85
	v_mov_b32_e32 v102, s88
	v_mov_b32_e32 v103, s87
	v_mov_b32_e32 v104, s90
	v_mov_b32_e32 v105, s89
	v_mov_b32_e32 v106, s92
	v_mov_b32_e32 v107, s91
	v_mul_f32_e32 v32, v32, v73
	v_mov_b32_e32 v72, s9
	v_mov_b32_e32 v73, s8
	v_cndmask_b32_e64 v82, v84, v85, s[4:5]
	v_cndmask_b32_e64 v83, v86, v87, s[4:5]
	v_cndmask_b32_e64 v84, v88, v89, s[4:5]
	v_cndmask_b32_e64 v85, v90, v91, s[4:5]
	v_cndmask_b32_e64 v86, v92, v93, s[4:5]
	v_cndmask_b32_e64 v87, v94, v95, s[4:5]
	v_cndmask_b32_e64 v88, v96, v97, s[4:5]
	v_cndmask_b32_e64 v89, v98, v99, s[4:5]
	v_cndmask_b32_e64 v90, v100, v101, s[4:5]
	v_cndmask_b32_e64 v91, v102, v103, s[4:5]
	v_cndmask_b32_e64 v92, v104, v105, s[4:5]
	v_cndmask_b32_e64 v93, v106, v107, s[4:5]
	v_cndmask_b32_e64 v72, v72, v73, s[4:5]
	v_mul_f32_e32 v4, v4, v82
	v_mul_f32_e32 v5, v5, v83
	v_mul_f32_e32 v6, v6, v84
	v_mul_f32_e32 v7, v7, v85
	v_mul_f32_e32 v8, v8, v86
	v_mul_f32_e32 v9, v9, v87
	v_mul_f32_e32 v10, v10, v88
	v_mul_f32_e32 v11, v11, v89
	v_mul_f32_e32 v12, v12, v90
	v_mul_f32_e32 v13, v13, v91
	v_mul_f32_e32 v14, v14, v92
	v_mul_f32_e32 v15, v15, v93
	v_mul_f32_e32 v33, v33, v72

; __device__ __forceinline__ void cvt_load(const CvtItem& it, float (&v)[32], int lane) {
; #pragma unroll
;     for (int i = 0; i < 32; ++i) { const int kk = 2 * i + (lane >> 5); v[i] = it.W[(size_t)(it.k0 + kk) * it.N + it.n0 + (lane & 31)]; }
; }
; template <int PH, bool PRB = false>
; __device__ __forceinline__ void run_phase(int layer, LAS unsigned char* lds, const int wv_) {
;     ...
;                 for (;;) { const int gn = gi + NGW; const bool more = gn < NITEMS; CvtItem nxt = item_of(more ? gn : gi); float vn[32];
;                     if (more) cvt_load(nxt, vn, lane);
.LBB0_133:
	s_ashr_i32 s51, s50, 31
	s_lshl_b64 s[54:55], s[50:51], 2
	v_add_u32_e32 v81, s73, v67
	s_add_u32 s54, s56, s54
	s_addc_u32 s55, s57, s55
	v_ashrrev_i32_e32 v34, 31, v81
	v_lshl_add_u64 v[58:59], s[54:55], 0, v[68:69]
	v_mul_lo_u32 v36, s8, v34
	v_mul_lo_u32 v37, s9, v81
	v_mad_u64_u32 v[34:35], s[54:55], s8, v81, 0
	v_add3_u32 v35, v35, v36, v37
	v_add_u32_e32 v36, 2, v81
	v_ashrrev_i32_e32 v37, 31, v36
	v_mul_lo_u32 v38, s8, v37
	v_mul_lo_u32 v39, s9, v36
	v_mad_u64_u32 v[36:37], s[54:55], s8, v36, 0
	v_add3_u32 v37, v37, v38, v39
	v_add_u32_e32 v38, 4, v81
	v_ashrrev_i32_e32 v39, 31, v38
	v_mul_lo_u32 v40, s8, v39
	v_mul_lo_u32 v41, s9, v38
	v_mad_u64_u32 v[38:39], s[54:55], s8, v38, 0
	v_add3_u32 v39, v39, v40, v41
	v_add_u32_e32 v40, 6, v81
	v_ashrrev_i32_e32 v41, 31, v40
	v_mul_lo_u32 v42, s8, v41
	v_mul_lo_u32 v43, s9, v40
	v_mad_u64_u32 v[40:41], s[54:55], s8, v40, 0
	v_add3_u32 v41, v41, v42, v43
	v_add_u32_e32 v42, 8, v81
	v_ashrrev_i32_e32 v43, 31, v42
	v_mul_lo_u32 v44, s8, v43
	v_mul_lo_u32 v45, s9, v42
	v_mad_u64_u32 v[42:43], s[54:55], s8, v42, 0
	v_add3_u32 v43, v43, v44, v45
	v_add_u32_e32 v44, 10, v81
	v_ashrrev_i32_e32 v45, 31, v44
	v_mul_lo_u32 v46, s8, v45
	v_mul_lo_u32 v47, s9, v44
	v_mad_u64_u32 v[44:45], s[54:55], s8, v44, 0
	v_add3_u32 v45, v45, v46, v47
	v_add_u32_e32 v46, 12, v81
	v_ashrrev_i32_e32 v47, 31, v46
	v_mul_lo_u32 v48, s8, v47
	v_mul_lo_u32 v49, s9, v46
	v_mad_u64_u32 v[46:47], s[54:55], s8, v46, 0
	v_add3_u32 v47, v47, v48, v49
	v_add_u32_e32 v48, 14, v81
	v_ashrrev_i32_e32 v49, 31, v48
	v_mul_lo_u32 v50, s8, v49
	v_mul_lo_u32 v51, s9, v48
	v_mad_u64_u32 v[48:49], s[54:55], s8, v48, 0
	v_lshl_add_u64 v[34:35], v[34:35], 2, v[58:59]
	v_lshl_add_u64 v[36:37], v[36:37], 2, v[58:59]
	v_lshl_add_u64 v[38:39], v[38:39], 2, v[58:59]
	v_lshl_add_u64 v[40:41], v[40:41], 2, v[58:59]
	v_lshl_add_u64 v[42:43], v[42:43], 2, v[58:59]
	v_add3_u32 v49, v49, v50, v51
	v_lshl_add_u64 v[44:45], v[44:45], 2, v[58:59]
	v_lshl_add_u64 v[46:47], v[46:47], 2, v[58:59]
	v_lshl_add_u64 v[48:49], v[48:49], 2, v[58:59]
	global_load_dword v34, v[34:35], off nt
	s_nop 0
	global_load_dword v35, v[36:37], off nt
	s_nop 0
	global_load_dword v36, v[38:39], off nt
	global_load_dword v37, v[40:41], off nt
	s_nop 0
	global_load_dword v38, v[42:43], off nt
	global_load_dword v39, v[44:45], off nt
	global_load_dword v40, v[46:47], off nt
	global_load_dword v41, v[48:49], off nt
	v_add_u32_e32 v42, 16, v81
	v_ashrrev_i32_e32 v43, 31, v42
	v_mul_lo_u32 v44, s8, v43
	v_mul_lo_u32 v45, s9, v42
	v_mad_u64_u32 v[42:43], s[54:55], s8, v42, 0
	v_add3_u32 v43, v43, v44, v45
	v_add_u32_e32 v44, 18, v81
	v_ashrrev_i32_e32 v45, 31, v44
	v_mul_lo_u32 v46, s8, v45
	v_mul_lo_u32 v47, s9, v44
	v_mad_u64_u32 v[44:45], s[54:55], s8, v44, 0
	v_add3_u32 v45, v45, v46, v47
	v_add_u32_e32 v46, 20, v81
	v_ashrrev_i32_e32 v47, 31, v46
	v_mul_lo_u32 v48, s8, v47
	v_mul_lo_u32 v49, s9, v46
	v_mad_u64_u32 v[46:47], s[54:55], s8, v46, 0
	v_add3_u32 v47, v47, v48, v49
	v_add_u32_e32 v48, 22, v81
	v_ashrrev_i32_e32 v49, 31, v48
	v_mul_lo_u32 v50, s8, v49
	v_mul_lo_u32 v51, s9, v48
	v_mad_u64_u32 v[48:49], s[54:55], s8, v48, 0
	v_add3_u32 v49, v49, v50, v51
	v_add_u32_e32 v50, 24, v81
	v_ashrrev_i32_e32 v51, 31, v50
	v_mul_lo_u32 v52, s8, v51
	v_mul_lo_u32 v53, s9, v50
	v_mad_u64_u32 v[50:51], s[54:55], s8, v50, 0
	v_add3_u32 v51, v51, v52, v53
	v_add_u32_e32 v52, 26, v81
	v_ashrrev_i32_e32 v53, 31, v52
	v_mul_lo_u32 v54, s8, v53
	v_mul_lo_u32 v55, s9, v52
	v_mad_u64_u32 v[52:53], s[54:55], s8, v52, 0
	v_add3_u32 v53, v53, v54, v55
	v_add_u32_e32 v54, 28, v81
	v_ashrrev_i32_e32 v55, 31, v54
	v_mul_lo_u32 v56, s8, v55
	v_mul_lo_u32 v57, s9, v54
	v_mad_u64_u32 v[54:55], s[54:55], s8, v54, 0
	v_add3_u32 v55, v55, v56, v57
	v_add_u32_e32 v56, 30, v81
	v_ashrrev_i32_e32 v57, 31, v56
	v_mul_lo_u32 v60, s8, v57
	v_mul_lo_u32 v61, s9, v56
	v_mad_u64_u32 v[56:57], s[54:55], s8, v56, 0
	v_lshl_add_u64 v[42:43], v[42:43], 2, v[58:59]
	v_lshl_add_u64 v[44:45], v[44:45], 2, v[58:59]
	v_lshl_add_u64 v[46:47], v[46:47], 2, v[58:59]
	v_lshl_add_u64 v[48:49], v[48:49], 2, v[58:59]
	v_lshl_add_u64 v[50:51], v[50:51], 2, v[58:59]
	v_add3_u32 v57, v57, v60, v61
	v_lshl_add_u64 v[52:53], v[52:53], 2, v[58:59]
	v_lshl_add_u64 v[54:55], v[54:55], 2, v[58:59]
	v_lshl_add_u64 v[56:57], v[56:57], 2, v[58:59]
	global_load_dword v42, v[42:43], off nt
	s_nop 0
	global_load_dword v43, v[44:45], off nt
	s_nop 0
	global_load_dword v44, v[46:47], off nt
	global_load_dword v45, v[48:49], off nt
	s_nop 0
	global_load_dword v46, v[50:51], off nt
	global_load_dword v47, v[52:53], off nt
	global_load_dword v48, v[54:55], off nt
	global_load_dword v49, v[56:57], off nt
	v_add_u32_e32 v50, 32, v81
	v_ashrrev_i32_e32 v51, 31, v50
	v_mul_lo_u32 v52, s8, v51
	v_mul_lo_u32 v53, s9, v50
	v_mad_u64_u32 v[50:51], s[54:55], s8, v50, 0
	v_add3_u32 v51, v51, v52, v53
	v_add_u32_e32 v52, 34, v81
	v_ashrrev_i32_e32 v53, 31, v52
	v_mul_lo_u32 v54, s8, v53
	v_mul_lo_u32 v55, s9, v52
	v_mad_u64_u32 v[52:53], s[54:55], s8, v52, 0
	v_add3_u32 v53, v53, v54, v55
	v_add_u32_e32 v54, 36, v81
	v_ashrrev_i32_e32 v55, 31, v54
	v_mul_lo_u32 v56, s8, v55
	v_mul_lo_u32 v57, s9, v54
	v_mad_u64_u32 v[54:55], s[54:55], s8, v54, 0
	v_add3_u32 v55, v55, v56, v57
	v_add_u32_e32 v56, 38, v81
	v_ashrrev_i32_e32 v57, 31, v56
	v_mul_lo_u32 v60, s8, v57
	v_mul_lo_u32 v61, s9, v56
	v_mad_u64_u32 v[56:57], s[54:55], s8, v56, 0
	v_add3_u32 v57, v57, v60, v61
	v_add_u32_e32 v60, 40, v81
	v_ashrrev_i32_e32 v61, 31, v60
	v_mul_lo_u32 v62, s8, v61
	v_mul_lo_u32 v63, s9, v60
	v_mad_u64_u32 v[60:61], s[54:55], s8, v60, 0
	v_add3_u32 v61, v61, v62, v63
	v_add_u32_e32 v62, 42, v81
	v_ashrrev_i32_e32 v63, 31, v62
	v_mul_lo_u32 v64, s8, v63
	v_mul_lo_u32 v65, s9, v62
	v_mad_u64_u32 v[62:63], s[54:55], s8, v62, 0
	v_add3_u32 v63, v63, v64, v65
	v_add_u32_e32 v64, 44, v81
	v_ashrrev_i32_e32 v65, 31, v64
	v_mul_lo_u32 v72, s8, v65
	v_mul_lo_u32 v73, s9, v64
	v_mad_u64_u32 v[64:65], s[54:55], s8, v64, 0
	v_add3_u32 v65, v65, v72, v73
	v_add_u32_e32 v72, 46, v81
	v_ashrrev_i32_e32 v73, 31, v72
	s_waitcnt lgkmcnt(0)
; __device__ __forceinline__ void cvt_load(const CvtItem& it, float (&v)[32], int lane) {
; #pragma unroll
;     for (int i = 0; i < 32; ++i) { const int kk = 2 * i + (lane >> 5); v[i] = it.W[(size_t)(it.k0 + kk) * it.N + it.n0 + (lane & 31)]; }
; }
; template <int PH, bool PRB = false>
; __device__ __forceinline__ void run_phase(int layer, LAS unsigned char* lds, const int wv_) {
;     ...
;                 for (;;) { const int gn = gi + NGW; const bool more = gn < NITEMS; CvtItem nxt = item_of(more ? gn : gi); float vn[32];
;                     if (more) cvt_load(nxt, vn, lane);
;                     cvt_finish(cur, v, scr, lane);
	v_mul_lo_u32 v82, s8, v73
	v_mul_lo_u32 v83, s9, v72
	v_mad_u64_u32 v[72:73], s[54:55], s8, v72, 0
	v_lshl_add_u64 v[50:51], v[50:51], 2, v[58:59]
	v_lshl_add_u64 v[52:53], v[52:53], 2, v[58:59]
	v_lshl_add_u64 v[54:55], v[54:55], 2, v[58:59]
	v_lshl_add_u64 v[56:57], v[56:57], 2, v[58:59]
	v_lshl_add_u64 v[60:61], v[60:61], 2, v[58:59]
	v_add3_u32 v73, v73, v82, v83
	v_lshl_add_u64 v[62:63], v[62:63], 2, v[58:59]
	v_lshl_add_u64 v[64:65], v[64:65], 2, v[58:59]
	v_lshl_add_u64 v[72:73], v[72:73], 2, v[58:59]
	global_load_dword v50, v[50:51], off nt
	s_nop 0
	global_load_dword v51, v[52:53], off nt
	s_nop 0
	global_load_dword v52, v[54:55], off nt
	global_load_dword v53, v[56:57], off nt
	s_nop 0
	global_load_dword v54, v[60:61], off nt
	global_load_dword v55, v[62:63], off nt
	global_load_dword v56, v[64:65], off nt
	global_load_dword v57, v[72:73], off nt
	v_add_u32_e32 v60, 48, v81
	v_ashrrev_i32_e32 v61, 31, v60
	v_mul_lo_u32 v62, s8, v61
	v_mul_lo_u32 v63, s9, v60
	v_mad_u64_u32 v[60:61], s[54:55], s8, v60, 0
	v_add3_u32 v61, v61, v62, v63
	v_add_u32_e32 v62, 50, v81
	v_ashrrev_i32_e32 v63, 31, v62
	v_mul_lo_u32 v64, s8, v63
	v_mul_lo_u32 v65, s9, v62
	v_mad_u64_u32 v[62:63], s[54:55], s8, v62, 0
	v_add3_u32 v63, v63, v64, v65
	v_add_u32_e32 v64, 52, v81
	v_ashrrev_i32_e32 v65, 31, v64
	v_mul_lo_u32 v72, s8, v65
	v_mul_lo_u32 v73, s9, v64
	v_mad_u64_u32 v[64:65], s[54:55], s8, v64, 0
	v_add3_u32 v65, v65, v72, v73
	v_add_u32_e32 v72, 54, v81
	v_ashrrev_i32_e32 v73, 31, v72
	v_mul_lo_u32 v82, s8, v73
	v_mul_lo_u32 v83, s9, v72
	v_mad_u64_u32 v[72:73], s[54:55], s8, v72, 0
	v_add3_u32 v73, v73, v82, v83
	v_add_u32_e32 v82, 56, v81
	v_ashrrev_i32_e32 v83, 31, v82
	v_mul_lo_u32 v84, s8, v83
	v_mul_lo_u32 v85, s9, v82
	v_mad_u64_u32 v[82:83], s[54:55], s8, v82, 0
	v_add3_u32 v83, v83, v84, v85
	v_add_u32_e32 v84, 58, v81
	v_ashrrev_i32_e32 v85, 31, v84
	v_mul_lo_u32 v86, s8, v85
	v_mul_lo_u32 v87, s9, v84
	v_mad_u64_u32 v[84:85], s[54:55], s8, v84, 0
	v_add3_u32 v85, v85, v86, v87
	v_add_u32_e32 v86, 60, v81
	v_ashrrev_i32_e32 v87, 31, v86
	v_mul_lo_u32 v88, s8, v87
	v_mul_lo_u32 v89, s9, v86
	v_mad_u64_u32 v[86:87], s[54:55], s8, v86, 0
	v_add_u32_e32 v81, 62, v81
	v_add3_u32 v87, v87, v88, v89
	v_ashrrev_i32_e32 v88, 31, v81
	v_mul_lo_u32 v90, s8, v88
	v_mul_lo_u32 v91, s9, v81
	v_mad_u64_u32 v[88:89], s[8:9], s8, v81, 0
	v_lshl_add_u64 v[60:61], v[60:61], 2, v[58:59]
	v_lshl_add_u64 v[62:63], v[62:63], 2, v[58:59]
	v_lshl_add_u64 v[64:65], v[64:65], 2, v[58:59]
	v_add3_u32 v89, v89, v90, v91
	v_lshl_add_u64 v[72:73], v[72:73], 2, v[58:59]
	v_lshl_add_u64 v[82:83], v[82:83], 2, v[58:59]
	v_lshl_add_u64 v[84:85], v[84:85], 2, v[58:59]
	v_lshl_add_u64 v[86:87], v[86:87], 2, v[58:59]
	v_lshl_add_u64 v[88:89], v[88:89], 2, v[58:59]
	global_load_dword v58, v[60:61], off nt
	global_load_dword v59, v[62:63], off nt
	s_nop 0
	global_load_dword v60, v[64:65], off nt
	global_load_dword v61, v[72:73], off nt
	global_load_dword v62, v[82:83], off nt
	global_load_dword v63, v[84:85], off nt
	s_nop 0
	global_load_dword v64, v[86:87], off nt
	global_load_dword v65, v[88:89], off nt
	s_cmp_eq_u64 s[42:43], 0
	s_cbranch_scc0 .LBB0_129
	s_branch .LBB0_130

; __device__ __forceinline__ void cvt_load(const CvtItem& it, float (&v)[32], int lane) {
; #pragma unroll
;     for (int i = 0; i < 32; ++i) { const int kk = 2 * i + (lane >> 5); v[i] = it.W[(size_t)(it.k0 + kk) * it.N + it.n0 + (lane & 31)]; }
; }
; template <int PH, bool PRB = false>
; __device__ __forceinline__ void run_phase(int layer, LAS unsigned char* lds, const int wv_) {
;     ...
;         int gi = lo + cgw;
;         if (gi < hi) { CvtItem cur = item_of(gi); float v[32]; cvt_load(cur, v, lane);
.LBB0_1009:
	s_lshl_b64 s[24:25], s[50:51], 2
	v_bfe_u32 v72, v70, 5, 1
	v_and_b32_e32 v0, 31, v70
	s_add_u32 s10, s10, s24
	v_or_b32_e32 v1, s0, v72
	s_addc_u32 s11, s11, s25
	v_lshlrev_b32_e32 v64, 2, v0
	v_lshl_add_u64 v[2:3], s[10:11], 0, v[64:65]
	v_mul_hi_u32_u24_e32 v5, s6, v1
	v_mul_u32_u24_e32 v4, s6, v1
	v_lshl_add_u64 v[4:5], v[4:5], 2, v[2:3]
	global_load_dword v32, v[4:5], off nt
	v_or_b32_e32 v4, 2, v1
	v_mul_hi_u32_u24_e32 v5, s6, v4
	v_mul_u32_u24_e32 v4, s6, v4
	v_lshl_add_u64 v[4:5], v[4:5], 2, v[2:3]
	global_load_dword v33, v[4:5], off nt
	v_or_b32_e32 v4, 4, v1
	v_mul_hi_u32_u24_e32 v5, s6, v4
	v_mul_u32_u24_e32 v4, s6, v4
	v_lshl_add_u64 v[4:5], v[4:5], 2, v[2:3]
	global_load_dword v34, v[4:5], off nt
	v_or_b32_e32 v4, 6, v1
	v_mul_hi_u32_u24_e32 v5, s6, v4
	v_mul_u32_u24_e32 v4, s6, v4
	v_lshl_add_u64 v[4:5], v[4:5], 2, v[2:3]
	global_load_dword v35, v[4:5], off nt
	v_or_b32_e32 v4, 8, v1
	v_mul_hi_u32_u24_e32 v5, s6, v4
	v_mul_u32_u24_e32 v4, s6, v4
	v_lshl_add_u64 v[4:5], v[4:5], 2, v[2:3]
	global_load_dword v36, v[4:5], off nt
	v_or_b32_e32 v4, 10, v1
	v_mul_hi_u32_u24_e32 v5, s6, v4
	v_mul_u32_u24_e32 v4, s6, v4
	v_lshl_add_u64 v[4:5], v[4:5], 2, v[2:3]
	global_load_dword v37, v[4:5], off nt
	v_or_b32_e32 v4, 12, v1
	v_mul_hi_u32_u24_e32 v5, s6, v4
	v_mul_u32_u24_e32 v4, s6, v4
	v_lshl_add_u64 v[4:5], v[4:5], 2, v[2:3]
	global_load_dword v38, v[4:5], off nt
	v_or_b32_e32 v4, 14, v1
	v_mul_hi_u32_u24_e32 v5, s6, v4
	v_mul_u32_u24_e32 v4, s6, v4
	v_lshl_add_u64 v[4:5], v[4:5], 2, v[2:3]
	global_load_dword v39, v[4:5], off nt
	v_or_b32_e32 v4, 16, v1
	v_mul_hi_u32_u24_e32 v5, s6, v4
	v_mul_u32_u24_e32 v4, s6, v4
	v_lshl_add_u64 v[4:5], v[4:5], 2, v[2:3]
	global_load_dword v40, v[4:5], off nt
	v_or_b32_e32 v4, 18, v1
	v_mul_hi_u32_u24_e32 v5, s6, v4
	v_mul_u32_u24_e32 v4, s6, v4
	v_lshl_add_u64 v[4:5], v[4:5], 2, v[2:3]
	global_load_dword v41, v[4:5], off nt
	v_or_b32_e32 v4, 20, v1
	v_mul_hi_u32_u24_e32 v5, s6, v4
	v_mul_u32_u24_e32 v4, s6, v4
	v_lshl_add_u64 v[4:5], v[4:5], 2, v[2:3]
	global_load_dword v42, v[4:5], off nt
	v_or_b32_e32 v4, 22, v1
	v_mul_hi_u32_u24_e32 v5, s6, v4
	v_mul_u32_u24_e32 v4, s6, v4
	v_lshl_add_u64 v[4:5], v[4:5], 2, v[2:3]
	global_load_dword v43, v[4:5], off nt
	v_or_b32_e32 v4, 24, v1
	v_mul_hi_u32_u24_e32 v5, s6, v4
	v_mul_u32_u24_e32 v4, s6, v4
	v_lshl_add_u64 v[4:5], v[4:5], 2, v[2:3]
	global_load_dword v44, v[4:5], off nt
	v_or_b32_e32 v4, 26, v1
	v_mul_hi_u32_u24_e32 v5, s6, v4
	v_mul_u32_u24_e32 v4, s6, v4
	v_lshl_add_u64 v[4:5], v[4:5], 2, v[2:3]
	global_load_dword v45, v[4:5], off nt
	v_or_b32_e32 v4, 28, v1
	v_mul_hi_u32_u24_e32 v5, s6, v4
	v_mul_u32_u24_e32 v4, s6, v4
	v_lshl_add_u64 v[4:5], v[4:5], 2, v[2:3]
	global_load_dword v46, v[4:5], off nt
	v_or_b32_e32 v4, 30, v1
	v_mul_hi_u32_u24_e32 v5, s6, v4
	v_mul_u32_u24_e32 v4, s6, v4
	v_lshl_add_u64 v[4:5], v[4:5], 2, v[2:3]
	global_load_dword v47, v[4:5], off nt
	v_or_b32_e32 v4, 32, v1
	v_mul_hi_u32_u24_e32 v5, s6, v4
	v_mul_u32_u24_e32 v4, s6, v4
	v_lshl_add_u64 v[4:5], v[4:5], 2, v[2:3]
	global_load_dword v48, v[4:5], off nt
	v_or_b32_e32 v4, 34, v1
	v_mul_hi_u32_u24_e32 v5, s6, v4
	v_mul_u32_u24_e32 v4, s6, v4
	v_lshl_add_u64 v[4:5], v[4:5], 2, v[2:3]
	global_load_dword v49, v[4:5], off nt
	v_or_b32_e32 v4, 36, v1
	v_mul_hi_u32_u24_e32 v5, s6, v4
	v_mul_u32_u24_e32 v4, s6, v4
	v_lshl_add_u64 v[4:5], v[4:5], 2, v[2:3]
	global_load_dword v50, v[4:5], off nt
	v_or_b32_e32 v4, 38, v1
	v_mul_hi_u32_u24_e32 v5, s6, v4
	v_mul_u32_u24_e32 v4, s6, v4
	v_lshl_add_u64 v[4:5], v[4:5], 2, v[2:3]
	global_load_dword v51, v[4:5], off nt
	v_or_b32_e32 v4, 40, v1
	v_mul_hi_u32_u24_e32 v5, s6, v4
	v_mul_u32_u24_e32 v4, s6, v4
	v_lshl_add_u64 v[4:5], v[4:5], 2, v[2:3]
	global_load_dword v52, v[4:5], off nt
	v_or_b32_e32 v4, 42, v1
	v_mul_hi_u32_u24_e32 v5, s6, v4
	v_mul_u32_u24_e32 v4, s6, v4
	v_lshl_add_u64 v[4:5], v[4:5], 2, v[2:3]
	global_load_dword v53, v[4:5], off nt
	v_or_b32_e32 v4, 44, v1
	v_mul_hi_u32_u24_e32 v5, s6, v4
	v_mul_u32_u24_e32 v4, s6, v4
	v_lshl_add_u64 v[4:5], v[4:5], 2, v[2:3]
	global_load_dword v54, v[4:5], off nt
	v_or_b32_e32 v4, 46, v1
	v_mul_hi_u32_u24_e32 v5, s6, v4
	v_mul_u32_u24_e32 v4, s6, v4
	v_lshl_add_u64 v[4:5], v[4:5], 2, v[2:3]
	global_load_dword v55, v[4:5], off nt
	v_or_b32_e32 v4, 48, v1
	v_mul_hi_u32_u24_e32 v5, s6, v4
	v_mul_u32_u24_e32 v4, s6, v4
	v_lshl_add_u64 v[4:5], v[4:5], 2, v[2:3]
	global_load_dword v56, v[4:5], off nt
	v_or_b32_e32 v4, 50, v1
	v_mul_hi_u32_u24_e32 v5, s6, v4
	v_mul_u32_u24_e32 v4, s6, v4
	v_lshl_add_u64 v[4:5], v[4:5], 2, v[2:3]
	global_load_dword v57, v[4:5], off nt
	v_or_b32_e32 v4, 52, v1
	v_mul_hi_u32_u24_e32 v5, s6, v4
	v_mul_u32_u24_e32 v4, s6, v4
	v_lshl_add_u64 v[4:5], v[4:5], 2, v[2:3]
	global_load_dword v58, v[4:5], off nt
	v_or_b32_e32 v4, 54, v1
	v_mul_hi_u32_u24_e32 v5, s6, v4
	v_mul_u32_u24_e32 v4, s6, v4
	v_lshl_add_u64 v[4:5], v[4:5], 2, v[2:3]
	global_load_dword v59, v[4:5], off nt
	v_or_b32_e32 v4, 56, v1
	v_mul_hi_u32_u24_e32 v5, s6, v4
	v_mul_u32_u24_e32 v4, s6, v4
	v_lshl_add_u64 v[4:5], v[4:5], 2, v[2:3]
	global_load_dword v60, v[4:5], off nt
	v_or_b32_e32 v4, 58, v1
	v_mul_hi_u32_u24_e32 v5, s6, v4
	v_mul_u32_u24_e32 v4, s6, v4
	v_lshl_add_u64 v[4:5], v[4:5], 2, v[2:3]
	global_load_dword v61, v[4:5], off nt
	v_or_b32_e32 v4, 60, v1
	v_mul_hi_u32_u24_e32 v5, s6, v4
	v_mul_u32_u24_e32 v4, s6, v4
	v_lshl_add_u64 v[4:5], v[4:5], 2, v[2:3]
	v_or_b32_e32 v1, 62, v1
	global_load_dword v62, v[4:5], off nt
	v_mul_hi_u32_u24_e32 v5, s6, v1
	v_mul_u32_u24_e32 v4, s6, v1
	v_lshl_add_u64 v[2:3], v[4:5], 2, v[2:3]
	global_load_dword v63, v[2:3], off nt
	s_add_u32 s37, s4, s20
	v_lshlrev_b32_e32 v3, 3, v70
	v_readlane_b32 s6, v254, 9
	s_addc_u32 s38, s5, s21
	v_bfe_u32 v73, v70, 3, 3
	v_and_b32_e32 v66, 56, v3
	v_and_b32_e32 v71, 63, v70
	v_add_u32_e32 v1, s6, v64
	v_mul_u32_u24_e32 v2, 0x84, v72
	s_add_u32 s39, s16, 0x20400000
	v_mul_u32_u24_e32 v3, 0x84, v66
	v_lshlrev_b32_e32 v4, 2, v73
	s_addc_u32 s40, s17, 0
	v_cmp_gt_u32_e64 s[4:5], 32, v71
	v_add3_u32 v74, s6, v3, v4
	v_mov_b32_e32 v67, v65
	v_or_b32_e32 v75, 8, v73
	v_or_b32_e32 v76, 16, v73
	v_or_b32_e32 v77, 24, v73
	v_lshlrev_b32_e32 v64, 2, v0
	v_add_u32_e32 v78, v1, v2
	s_mov_b32 s46, s50
	s_waitcnt vmcnt(0)
	s_branch .LBB0_1011

; #define LAS __attribute__((address_space(3)))
; __device__ __forceinline__ void cvt_finish(const CvtItem& it, float (&v)[32], LAS float* scr, int lane) {
;     if (it.g) { const float gv = it.g[it.k0 + lane];
.LBB0_1011:
	s_cmp_eq_u64 s[8:9], 0
	s_cbranch_scc1 .Lcv_nog
	v_add_u32_e32 v84, s0, v71
	v_mov_b32_e32 v85, v65
	v_lshl_add_u64 v[84:85], v[84:85], 2, s[8:9]
	global_load_dword v82, v[84:85], off nt

; __device__ __forceinline__ void cvt_load(const CvtItem& it, float (&v)[32], int lane) {
; #pragma unroll
;     for (int i = 0; i < 32; ++i) { const int kk = 2 * i + (lane >> 5); v[i] = it.W[(size_t)(it.k0 + kk) * it.N + it.n0 + (lane & 31)]; }
; }
; template <int PH, bool PRB = false>
; __device__ __forceinline__ void run_phase(int layer, LAS unsigned char* lds, const int wv_) {
;     ...
;             for (;;) { const int gn = gi + CNGW; const bool more = gn < hi; CvtItem nxt = item_of(more ? gn : gi); float vn[32];
;                 if (more) cvt_load(nxt, vn, lane);
.LBB0_1016:
	s_lshl_b64 s[30:31], s[50:51], 2
	s_add_u32 s28, s28, s30
	v_or_b32_e32 v79, s41, v72
	s_addc_u32 s29, s29, s31
	v_lshl_add_u64 v[68:69], s[28:29], 0, v[64:65]
	v_mul_hi_u32_u24_e32 v1, s10, v79
	v_mul_u32_u24_e32 v0, s10, v79
	v_lshl_add_u64 v[0:1], v[0:1], 2, v[68:69]
	global_load_dword v0, v[0:1], off nt
	v_or_b32_e32 v1, 2, v79
	v_mul_hi_u32_u24_e32 v3, s10, v1
	v_mul_u32_u24_e32 v2, s10, v1
	v_lshl_add_u64 v[2:3], v[2:3], 2, v[68:69]
	global_load_dword v1, v[2:3], off nt
	v_or_b32_e32 v2, 4, v79
	v_mul_hi_u32_u24_e32 v3, s10, v2
	v_mul_u32_u24_e32 v2, s10, v2
	v_lshl_add_u64 v[2:3], v[2:3], 2, v[68:69]
	global_load_dword v2, v[2:3], off nt
	v_or_b32_e32 v3, 6, v79
	v_mul_hi_u32_u24_e32 v5, s10, v3
	v_mul_u32_u24_e32 v4, s10, v3
	v_lshl_add_u64 v[4:5], v[4:5], 2, v[68:69]
	global_load_dword v3, v[4:5], off nt
	v_or_b32_e32 v4, 8, v79
	v_mul_hi_u32_u24_e32 v5, s10, v4
	v_mul_u32_u24_e32 v4, s10, v4
	v_lshl_add_u64 v[4:5], v[4:5], 2, v[68:69]
	global_load_dword v4, v[4:5], off nt
	v_or_b32_e32 v5, 10, v79
	v_mul_hi_u32_u24_e32 v7, s10, v5
	v_mul_u32_u24_e32 v6, s10, v5
	v_lshl_add_u64 v[6:7], v[6:7], 2, v[68:69]
	global_load_dword v5, v[6:7], off nt
	v_or_b32_e32 v6, 12, v79
	v_mul_hi_u32_u24_e32 v7, s10, v6
	v_mul_u32_u24_e32 v6, s10, v6
	v_lshl_add_u64 v[6:7], v[6:7], 2, v[68:69]
	global_load_dword v6, v[6:7], off nt
	v_or_b32_e32 v7, 14, v79
	v_mul_hi_u32_u24_e32 v9, s10, v7
	v_mul_u32_u24_e32 v8, s10, v7
	v_lshl_add_u64 v[8:9], v[8:9], 2, v[68:69]
	global_load_dword v7, v[8:9], off nt
	v_or_b32_e32 v8, 16, v79
	v_mul_hi_u32_u24_e32 v9, s10, v8
	v_mul_u32_u24_e32 v8, s10, v8
	v_lshl_add_u64 v[8:9], v[8:9], 2, v[68:69]
	global_load_dword v8, v[8:9], off nt
	v_or_b32_e32 v9, 18, v79
	s_waitcnt vmcnt(42)
	v_mul_hi_u32_u24_e32 v11, s10, v9
	v_mul_u32_u24_e32 v10, s10, v9
	v_lshl_add_u64 v[10:11], v[10:11], 2, v[68:69]
	global_load_dword v9, v[10:11], off nt
	v_or_b32_e32 v10, 20, v79
	v_mul_hi_u32_u24_e32 v11, s10, v10
	v_mul_u32_u24_e32 v10, s10, v10
	v_lshl_add_u64 v[10:11], v[10:11], 2, v[68:69]
	global_load_dword v10, v[10:11], off nt
	v_or_b32_e32 v11, 22, v79
	v_mul_hi_u32_u24_e32 v13, s10, v11
	v_mul_u32_u24_e32 v12, s10, v11
	v_lshl_add_u64 v[12:13], v[12:13], 2, v[68:69]
	global_load_dword v11, v[12:13], off nt
	v_or_b32_e32 v12, 24, v79
	v_mul_hi_u32_u24_e32 v13, s10, v12
	v_mul_u32_u24_e32 v12, s10, v12
	v_lshl_add_u64 v[12:13], v[12:13], 2, v[68:69]
	global_load_dword v12, v[12:13], off nt
	v_or_b32_e32 v13, 26, v79
	v_mul_hi_u32_u24_e32 v15, s10, v13
	v_mul_u32_u24_e32 v14, s10, v13
	v_lshl_add_u64 v[14:15], v[14:15], 2, v[68:69]
	global_load_dword v13, v[14:15], off nt
	v_or_b32_e32 v14, 28, v79
	v_mul_hi_u32_u24_e32 v15, s10, v14
	v_mul_u32_u24_e32 v14, s10, v14
	v_lshl_add_u64 v[14:15], v[14:15], 2, v[68:69]
	global_load_dword v14, v[14:15], off nt
	v_or_b32_e32 v15, 30, v79
	v_mul_hi_u32_u24_e32 v17, s10, v15
	v_mul_u32_u24_e32 v16, s10, v15
	v_lshl_add_u64 v[16:17], v[16:17], 2, v[68:69]
	global_load_dword v15, v[16:17], off nt
	v_or_b32_e32 v16, 32, v79
	v_mul_hi_u32_u24_e32 v17, s10, v16
	v_mul_u32_u24_e32 v16, s10, v16
	v_lshl_add_u64 v[16:17], v[16:17], 2, v[68:69]
	global_load_dword v16, v[16:17], off nt
	v_or_b32_e32 v17, 34, v79
	v_mul_hi_u32_u24_e32 v19, s10, v17
	v_mul_u32_u24_e32 v18, s10, v17
	v_lshl_add_u64 v[18:19], v[18:19], 2, v[68:69]
	global_load_dword v17, v[18:19], off nt
	v_or_b32_e32 v18, 36, v79
	v_mul_hi_u32_u24_e32 v19, s10, v18
	v_mul_u32_u24_e32 v18, s10, v18
	v_lshl_add_u64 v[18:19], v[18:19], 2, v[68:69]
	global_load_dword v18, v[18:19], off nt
	v_or_b32_e32 v19, 38, v79
	v_mul_hi_u32_u24_e32 v21, s10, v19
	v_mul_u32_u24_e32 v20, s10, v19
	v_lshl_add_u64 v[20:21], v[20:21], 2, v[68:69]
	global_load_dword v19, v[20:21], off nt
	v_or_b32_e32 v20, 40, v79
	v_mul_hi_u32_u24_e32 v21, s10, v20
	v_mul_u32_u24_e32 v20, s10, v20
	v_lshl_add_u64 v[20:21], v[20:21], 2, v[68:69]
	global_load_dword v20, v[20:21], off nt
	v_or_b32_e32 v21, 42, v79
	v_mul_hi_u32_u24_e32 v23, s10, v21
	v_mul_u32_u24_e32 v22, s10, v21
	v_lshl_add_u64 v[22:23], v[22:23], 2, v[68:69]
	global_load_dword v21, v[22:23], off nt
	v_or_b32_e32 v22, 44, v79
	v_mul_hi_u32_u24_e32 v23, s10, v22
	v_mul_u32_u24_e32 v22, s10, v22
	v_lshl_add_u64 v[22:23], v[22:23], 2, v[68:69]
	global_load_dword v22, v[22:23], off nt
	v_or_b32_e32 v23, 46, v79
	v_mul_hi_u32_u24_e32 v25, s10, v23
	v_mul_u32_u24_e32 v24, s10, v23
	v_lshl_add_u64 v[24:25], v[24:25], 2, v[68:69]
	global_load_dword v23, v[24:25], off nt
	v_or_b32_e32 v24, 48, v79
	v_mul_hi_u32_u24_e32 v25, s10, v24
	v_mul_u32_u24_e32 v24, s10, v24
	v_lshl_add_u64 v[24:25], v[24:25], 2, v[68:69]
	global_load_dword v24, v[24:25], off nt
	v_or_b32_e32 v25, 50, v79
	v_mul_hi_u32_u24_e32 v27, s10, v25
	v_mul_u32_u24_e32 v26, s10, v25
	v_lshl_add_u64 v[26:27], v[26:27], 2, v[68:69]
	global_load_dword v25, v[26:27], off nt
	v_or_b32_e32 v26, 52, v79
	v_mul_hi_u32_u24_e32 v27, s10, v26
	v_mul_u32_u24_e32 v26, s10, v26
	v_lshl_add_u64 v[26:27], v[26:27], 2, v[68:69]
	global_load_dword v26, v[26:27], off nt
	v_or_b32_e32 v27, 54, v79
	v_mul_hi_u32_u24_e32 v29, s10, v27
	v_mul_u32_u24_e32 v28, s10, v27
	v_lshl_add_u64 v[28:29], v[28:29], 2, v[68:69]
	global_load_dword v27, v[28:29], off nt
	v_or_b32_e32 v28, 56, v79
	v_mul_hi_u32_u24_e32 v29, s10, v28
	v_mul_u32_u24_e32 v28, s10, v28
	v_lshl_add_u64 v[28:29], v[28:29], 2, v[68:69]
	global_load_dword v28, v[28:29], off nt
	v_or_b32_e32 v29, 58, v79
	v_mul_hi_u32_u24_e32 v31, s10, v29
	v_mul_u32_u24_e32 v30, s10, v29
	v_lshl_add_u64 v[30:31], v[30:31], 2, v[68:69]
	global_load_dword v29, v[30:31], off nt
	v_or_b32_e32 v30, 60, v79
	v_mul_hi_u32_u24_e32 v31, s10, v30
	v_mul_u32_u24_e32 v30, s10, v30
	v_lshl_add_u64 v[30:31], v[30:31], 2, v[68:69]
	global_load_dword v30, v[30:31], off nt
	v_or_b32_e32 v31, 62, v79
	v_mul_hi_u32_u24_e32 v81, s10, v31
	v_mul_u32_u24_e32 v80, s10, v31
	v_lshl_add_u64 v[68:69], v[80:81], 2, v[68:69]
	global_load_dword v31, v[68:69], off nt
